# speedup vs baseline: 1.0053x; 1.0053x over previous
.Lg0_cloop:
	s_mul_i32 s8, s3, 0x7000
	s_barrier
	v_add_u32_e32 v103, s8, v100
	v_add_u32_e32 v101, s8, v99
	ds_read_b128 v[146:149], v103 offset:12288
	ds_read_b128 v[150:153], v103 offset:13312
	ds_read_b128 v[154:157], v103 offset:14336
	ds_read_b128 v[158:161], v103 offset:15360
	s_waitcnt lgkmcnt(9)
	v_mfma_f32_16x16x32_f16 v[94:97], v[122:125], v[104:107], v[94:97]
	s_add_i32 s8, s3, 1
	s_cmp_lg_u32 s3, 4
	s_cselect_b32 s3, s8, 0
	v_mfma_f32_16x16x32_f16 v[70:73], v[122:125], v[108:111], v[70:73]
	v_mfma_f32_16x16x32_f16 v[46:49], v[122:125], v[112:115], v[46:49]
	v_mfma_f32_16x16x32_f16 v[22:25], v[122:125], v[116:119], v[22:25]
	ds_read_b128 v[122:125], v101
	s_waitcnt lgkmcnt(9)
	v_mfma_f32_16x16x32_f16 v[90:93], v[126:129], v[104:107], v[90:93]
	v_mfma_f32_16x16x32_f16 v[66:69], v[126:129], v[108:111], v[66:69]
	v_mfma_f32_16x16x32_f16 v[42:45], v[126:129], v[112:115], v[42:45]
	v_mfma_f32_16x16x32_f16 v[18:21], v[126:129], v[116:119], v[18:21]
	ds_read_b128 v[126:129], v101 offset:1024
	s_waitcnt lgkmcnt(9)
	v_mfma_f32_16x16x32_f16 v[86:89], v[130:133], v[104:107], v[86:89]
	v_mfma_f32_16x16x32_f16 v[54:57], v[130:133], v[108:111], v[54:57]
	v_mfma_f32_16x16x32_f16 v[26:29], v[130:133], v[112:115], v[26:29]
	v_mfma_f32_16x16x32_f16 v[6:9], v[130:133], v[116:119], v[6:9]
	ds_read_b128 v[130:133], v101 offset:2048
	s_waitcnt lgkmcnt(9)
	v_mfma_f32_16x16x32_f16 v[74:77], v[134:137], v[104:107], v[74:77]
	v_mfma_f32_16x16x32_f16 v[50:53], v[134:137], v[108:111], v[50:53]
	v_mfma_f32_16x16x32_f16 v[38:41], v[134:137], v[112:115], v[38:41]
	v_mfma_f32_16x16x32_f16 v[14:17], v[134:137], v[116:119], v[14:17]
	ds_read_b128 v[134:137], v101 offset:3072
	s_waitcnt lgkmcnt(9)
	v_mfma_f32_16x16x32_f16 v[82:85], v[138:141], v[104:107], v[82:85]
	v_mfma_f32_16x16x32_f16 v[58:61], v[138:141], v[108:111], v[58:61]
	v_mfma_f32_16x16x32_f16 v[30:33], v[138:141], v[112:115], v[30:33]
	v_mfma_f32_16x16x32_f16 v[10:13], v[138:141], v[116:119], v[10:13]
	ds_read_b128 v[138:141], v101 offset:4096
	s_waitcnt lgkmcnt(9)
	v_mfma_f32_16x16x32_f16 v[78:81], v[142:145], v[104:107], v[78:81]
	v_mfma_f32_16x16x32_f16 v[62:65], v[142:145], v[108:111], v[62:65]
	v_mfma_f32_16x16x32_f16 v[34:37], v[142:145], v[112:115], v[34:37]
	v_mfma_f32_16x16x32_f16 v[2:5], v[142:145], v[116:119], v[2:5]
	ds_read_b128 v[142:145], v101 offset:5120
	s_mul_i32 s8, s3, 0x7000
	s_barrier
	v_add_u32_e32 v103, s8, v100
	v_add_u32_e32 v101, s8, v99
	ds_read_b128 v[104:107], v103 offset:12288
	ds_read_b128 v[108:111], v103 offset:13312
	ds_read_b128 v[112:115], v103 offset:14336
	ds_read_b128 v[116:119], v103 offset:15360
	s_waitcnt lgkmcnt(9)
	v_mfma_f32_16x16x32_f16 v[94:97], v[122:125], v[146:149], v[94:97]
	s_add_i32 s8, s3, 1
	s_cmp_lg_u32 s3, 4
	s_cselect_b32 s3, s8, 0
	v_mfma_f32_16x16x32_f16 v[70:73], v[122:125], v[150:153], v[70:73]
	v_mfma_f32_16x16x32_f16 v[46:49], v[122:125], v[154:157], v[46:49]
	v_mfma_f32_16x16x32_f16 v[22:25], v[122:125], v[158:161], v[22:25]
	ds_read_b128 v[122:125], v101
	s_waitcnt lgkmcnt(9)
	v_mfma_f32_16x16x32_f16 v[90:93], v[126:129], v[146:149], v[90:93]
	v_mfma_f32_16x16x32_f16 v[66:69], v[126:129], v[150:153], v[66:69]
	v_mfma_f32_16x16x32_f16 v[42:45], v[126:129], v[154:157], v[42:45]
	v_mfma_f32_16x16x32_f16 v[18:21], v[126:129], v[158:161], v[18:21]
	ds_read_b128 v[126:129], v101 offset:1024
	s_waitcnt lgkmcnt(9)
	v_mfma_f32_16x16x32_f16 v[86:89], v[130:133], v[146:149], v[86:89]
	v_mfma_f32_16x16x32_f16 v[54:57], v[130:133], v[150:153], v[54:57]
	v_mfma_f32_16x16x32_f16 v[26:29], v[130:133], v[154:157], v[26:29]
	v_mfma_f32_16x16x32_f16 v[6:9], v[130:133], v[158:161], v[6:9]
	ds_read_b128 v[130:133], v101 offset:2048
	s_waitcnt lgkmcnt(9)
	v_mfma_f32_16x16x32_f16 v[74:77], v[134:137], v[146:149], v[74:77]
	v_mfma_f32_16x16x32_f16 v[50:53], v[134:137], v[150:153], v[50:53]
	v_mfma_f32_16x16x32_f16 v[38:41], v[134:137], v[154:157], v[38:41]
	v_mfma_f32_16x16x32_f16 v[14:17], v[134:137], v[158:161], v[14:17]
	ds_read_b128 v[134:137], v101 offset:3072
	s_waitcnt lgkmcnt(9)
	v_mfma_f32_16x16x32_f16 v[82:85], v[138:141], v[146:149], v[82:85]
	v_mfma_f32_16x16x32_f16 v[58:61], v[138:141], v[150:153], v[58:61]
	v_mfma_f32_16x16x32_f16 v[30:33], v[138:141], v[154:157], v[30:33]
	v_mfma_f32_16x16x32_f16 v[10:13], v[138:141], v[158:161], v[10:13]
	ds_read_b128 v[138:141], v101 offset:4096
	s_waitcnt lgkmcnt(9)
	v_mfma_f32_16x16x32_f16 v[78:81], v[142:145], v[146:149], v[78:81]
	v_mfma_f32_16x16x32_f16 v[62:65], v[142:145], v[150:153], v[62:65]
	v_mfma_f32_16x16x32_f16 v[34:37], v[142:145], v[154:157], v[34:37]
	v_mfma_f32_16x16x32_f16 v[2:5], v[142:145], v[158:161], v[2:5]
	ds_read_b128 v[142:145], v101 offset:5120
	s_add_i32 s7, s7, -1
	s_cmp_eq_u32 s7, 0
	s_cbranch_scc0 .Lg0_cloop
	s_waitcnt lgkmcnt(0)
	s_barrier
	s_mul_i32 s24, s22, 0x3400
	s_lshl_b32 s28, s2, 6
	s_add_i32 s29, s20, s28
	s_and_b32 s30, s29, 0x7ff
	v_add_u32_e32 v98, s30, v102
	v_lshlrev_b32_e32 v98, 8, v98
	v_lshl_add_u32 v98, v120, 4, v98
	v_add_u32_e32 v99, 0x1000, v98
	v_add_u32_e32 v100, 0x2000, v98
	v_add_u32_e32 v101, 0x3000, v98
	v_mul_u32_u24_e32 v103, 0xd0, v102
	v_lshl_add_u32 v103, v120, 3, v103
	v_add_u32_e32 v103, s24, v103
	v_lshrrev_b32_e32 v0, 2, v1
	v_and_b32_e32 v1, 3, v1
	v_mul_u32_u24_e32 v102, 0xd0, v0
	v_lshl_add_u32 v102, v1, 4, v102
	v_add_u32_e32 v102, s24, v102
	v_lshlrev_b32_e32 v0, 11, v0
	v_lshl_add_u32 v0, v1, 4, v0
	s_lshl_b32 s31, s5, 7
	s_add_i32 s35, s31, 0
	s_and_b32 s35, s35, 0xff
	s_add_u32 s36, s12, s35
	s_addc_u32 s37, s13, 0
	s_add_i32 s35, s31, 64
	s_and_b32 s35, s35, 0xff
	s_add_u32 s38, s12, s35
	s_addc_u32 s39, s13, 0
	s_add_i32 s35, s31, 128
	s_and_b32 s35, s35, 0xff
	s_add_u32 s40, s12, s35
	s_addc_u32 s41, s13, 0
	s_add_i32 s35, s31, 192
	s_and_b32 s35, s35, 0xff
	s_add_u32 s42, s12, s35
	s_addc_u32 s43, s13, 0
	s_add_i32 s34, s25, s23
	s_sub_i32 s32, 0x400, s34
	s_ashr_i32 s32, s32, 4
	s_max_i32 s32, s32, 0
	s_min_i32 s32, s32, 6
	s_sub_i32 s33, 0x800, s34
	s_ashr_i32 s33, s33, 4
	s_max_i32 s33, s33, 0
	s_min_i32 s33, s33, 6
	s_cmp_eq_u32 s33, 0
	s_cbranch_scc1 .Lepi_noload
	global_load_dwordx4 v[108:111], v98, s[38:39]
	global_load_dwordx4 v[124:127], v99, s[38:39]
	global_load_dwordx4 v[140:143], v100, s[38:39]
	global_load_dwordx4 v[156:159], v101, s[38:39]
	global_load_dwordx4 v[104:107], v98, s[36:37]
	global_load_dwordx4 v[120:123], v99, s[36:37]
	global_load_dwordx4 v[136:139], v100, s[36:37]
	global_load_dwordx4 v[152:155], v101, s[36:37]
	global_load_dwordx4 v[116:119], v98, s[42:43]
	global_load_dwordx4 v[132:135], v99, s[42:43]
	global_load_dwordx4 v[148:151], v100, s[42:43]
	global_load_dwordx4 v[164:167], v101, s[42:43]
	global_load_dwordx4 v[112:115], v98, s[40:41]
	global_load_dwordx4 v[128:131], v99, s[40:41]
	global_load_dwordx4 v[144:147], v100, s[40:41]
	global_load_dwordx4 v[160:163], v101, s[40:41]
.Lepi_noload:
	s_cmp_le_u32 s33, 5
	s_cbranch_scc1 .Lepi_v5
	s_waitcnt vmcnt(12)
	s_cmp_le_u32 s32, 5
	s_cbranch_scc1 .Lepi_r5
	v_mul_f32_e32 v108, 0x3e38aa3b, v108
	v_mul_f32_e32 v109, 0x3e38aa3b, v109
	v_mul_f32_e32 v110, 0x3e38aa3b, v110
	v_mul_f32_e32 v111, 0x3e38aa3b, v111
	v_mul_f32_e32 v124, 0x3e38aa3b, v124
	v_mul_f32_e32 v125, 0x3e38aa3b, v125
	v_mul_f32_e32 v126, 0x3e38aa3b, v126
	v_mul_f32_e32 v127, 0x3e38aa3b, v127
	v_mul_f32_e32 v140, 0x3e38aa3b, v140
	v_mul_f32_e32 v141, 0x3e38aa3b, v141
	v_mul_f32_e32 v142, 0x3e38aa3b, v142
	v_mul_f32_e32 v143, 0x3e38aa3b, v143
	v_mul_f32_e32 v156, 0x3e38aa3b, v156
	v_mul_f32_e32 v157, 0x3e38aa3b, v157
	v_mul_f32_e32 v158, 0x3e38aa3b, v158
	v_mul_f32_e32 v159, 0x3e38aa3b, v159

.Lepi_d5:
	s_cmp_le_u32 s33, 4
	s_cbranch_scc1 .Lepi_v4
	s_waitcnt vmcnt(8)
	s_cmp_le_u32 s32, 4
	s_cbranch_scc1 .Lepi_r4
	v_mul_f32_e32 v104, 0x3e38aa3b, v104
	v_mul_f32_e32 v105, 0x3e38aa3b, v105
	v_mul_f32_e32 v106, 0x3e38aa3b, v106
	v_mul_f32_e32 v107, 0x3e38aa3b, v107
	v_mul_f32_e32 v120, 0x3e38aa3b, v120
	v_mul_f32_e32 v121, 0x3e38aa3b, v121
	v_mul_f32_e32 v122, 0x3e38aa3b, v122
	v_mul_f32_e32 v123, 0x3e38aa3b, v123
	v_mul_f32_e32 v136, 0x3e38aa3b, v136
	v_mul_f32_e32 v137, 0x3e38aa3b, v137
	v_mul_f32_e32 v138, 0x3e38aa3b, v138
	v_mul_f32_e32 v139, 0x3e38aa3b, v139
	v_mul_f32_e32 v152, 0x3e38aa3b, v152
	v_mul_f32_e32 v153, 0x3e38aa3b, v153
	v_mul_f32_e32 v154, 0x3e38aa3b, v154
	v_mul_f32_e32 v155, 0x3e38aa3b, v155

.Lepi_d4:
	s_cmp_le_u32 s33, 3
	s_cbranch_scc1 .Lepi_v3
	s_waitcnt vmcnt(4)
	s_cmp_le_u32 s32, 3
	s_cbranch_scc1 .Lepi_r3
	v_mul_f32_e32 v116, 0x3e38aa3b, v116
	v_mul_f32_e32 v117, 0x3e38aa3b, v117
	v_mul_f32_e32 v118, 0x3e38aa3b, v118
	v_mul_f32_e32 v119, 0x3e38aa3b, v119
	v_mul_f32_e32 v132, 0x3e38aa3b, v132
	v_mul_f32_e32 v133, 0x3e38aa3b, v133
	v_mul_f32_e32 v134, 0x3e38aa3b, v134
	v_mul_f32_e32 v135, 0x3e38aa3b, v135
	v_mul_f32_e32 v148, 0x3e38aa3b, v148
	v_mul_f32_e32 v149, 0x3e38aa3b, v149
	v_mul_f32_e32 v150, 0x3e38aa3b, v150
	v_mul_f32_e32 v151, 0x3e38aa3b, v151
	v_mul_f32_e32 v164, 0x3e38aa3b, v164
	v_mul_f32_e32 v165, 0x3e38aa3b, v165
	v_mul_f32_e32 v166, 0x3e38aa3b, v166
	v_mul_f32_e32 v167, 0x3e38aa3b, v167

.Lepi_d3:
	s_cmp_le_u32 s33, 2
	s_cbranch_scc1 .Lepi_v2
	s_waitcnt vmcnt(0)
	s_cmp_le_u32 s32, 2
	s_cbranch_scc1 .Lepi_r2
	v_mul_f32_e32 v112, 0x3e38aa3b, v112
	v_mul_f32_e32 v113, 0x3e38aa3b, v113
	v_mul_f32_e32 v114, 0x3e38aa3b, v114
	v_mul_f32_e32 v115, 0x3e38aa3b, v115
	v_mul_f32_e32 v128, 0x3e38aa3b, v128
	v_mul_f32_e32 v129, 0x3e38aa3b, v129
	v_mul_f32_e32 v130, 0x3e38aa3b, v130
	v_mul_f32_e32 v131, 0x3e38aa3b, v131
	v_mul_f32_e32 v144, 0x3e38aa3b, v144
	v_mul_f32_e32 v145, 0x3e38aa3b, v145
	v_mul_f32_e32 v146, 0x3e38aa3b, v146
	v_mul_f32_e32 v147, 0x3e38aa3b, v147
	v_mul_f32_e32 v160, 0x3e38aa3b, v160
	v_mul_f32_e32 v161, 0x3e38aa3b, v161
	v_mul_f32_e32 v162, 0x3e38aa3b, v162
	v_mul_f32_e32 v163, 0x3e38aa3b, v163

.Lepi_d2:
	s_cmp_le_u32 s33, 1
	s_cbranch_scc1 .Lepi_v1
	s_waitcnt vmcnt(0)
	s_cmp_le_u32 s32, 1
	s_cbranch_scc1 .Lepi_r1
	s_cmp_eq_u32 s32, 6
	s_cbranch_scc1 .Lepi_r1
	v_mul_f32_e32 v108, 0x3e38aa3b, v108
	v_mul_f32_e32 v109, 0x3e38aa3b, v109
	v_mul_f32_e32 v110, 0x3e38aa3b, v110
	v_mul_f32_e32 v111, 0x3e38aa3b, v111
	v_mul_f32_e32 v124, 0x3e38aa3b, v124
	v_mul_f32_e32 v125, 0x3e38aa3b, v125
	v_mul_f32_e32 v126, 0x3e38aa3b, v126
	v_mul_f32_e32 v127, 0x3e38aa3b, v127
	v_mul_f32_e32 v140, 0x3e38aa3b, v140
	v_mul_f32_e32 v141, 0x3e38aa3b, v141
	v_mul_f32_e32 v142, 0x3e38aa3b, v142
	v_mul_f32_e32 v143, 0x3e38aa3b, v143
	v_mul_f32_e32 v156, 0x3e38aa3b, v156
	v_mul_f32_e32 v157, 0x3e38aa3b, v157
	v_mul_f32_e32 v158, 0x3e38aa3b, v158
	v_mul_f32_e32 v159, 0x3e38aa3b, v159

.Lepi_d1:
	s_cmp_le_u32 s33, 0
	s_cbranch_scc1 .Lepi_v0
	s_waitcnt vmcnt(0)
	s_cmp_le_u32 s32, 0
	s_cbranch_scc1 .Lepi_r0
	s_cmp_ge_u32 s32, 5
	s_cbranch_scc1 .Lepi_r0
	v_mul_f32_e32 v104, 0x3e38aa3b, v104
	v_mul_f32_e32 v105, 0x3e38aa3b, v105
	v_mul_f32_e32 v106, 0x3e38aa3b, v106
	v_mul_f32_e32 v107, 0x3e38aa3b, v107
	v_mul_f32_e32 v120, 0x3e38aa3b, v120
	v_mul_f32_e32 v121, 0x3e38aa3b, v121
	v_mul_f32_e32 v122, 0x3e38aa3b, v122
	v_mul_f32_e32 v123, 0x3e38aa3b, v123
	v_mul_f32_e32 v136, 0x3e38aa3b, v136
	v_mul_f32_e32 v137, 0x3e38aa3b, v137
	v_mul_f32_e32 v138, 0x3e38aa3b, v138
	v_mul_f32_e32 v139, 0x3e38aa3b, v139
	v_mul_f32_e32 v152, 0x3e38aa3b, v152
	v_mul_f32_e32 v153, 0x3e38aa3b, v153
	v_mul_f32_e32 v154, 0x3e38aa3b, v154
	v_mul_f32_e32 v155, 0x3e38aa3b, v155
